# v91 + k6 LN1 row-sum exchange: dropped the L1 invalidate after the partner poll (partner sums and router partials are read with agent-scope sc1 loads)
# baseline (speedup 1.0000x reference)
.LBB0_1028:
	s_and_b64 s[8:9], exec, s[42:43]
	v_readlane_b32 s74, v254, 63
	v_readlane_b32 s75, v255, 2
	s_mov_b64 exec, s[8:9]
	s_add_i32 s8, 0, 0x27800
	v_cndmask_b32_e64 v60, 0, 1, s[70:71]
	v_mov_b32_e32 v61, s8
	ds_write_b32 v61, v60
